# baseline (speedup 1.0000x reference)
.Lstag_done_p3:
	s_mov_b32 s66, s2
	s_load_dwordx2 s[64:65], s[0:1], 0x0
	v_lshrrev_b32_e32 v162, 6, v0
	v_bfe_u32 v163, v0, 2, 4
	v_lshl_add_u32 v162, v162, 7, v163
	v_lshlrev_b32_e32 v163, 4, v0
	v_and_b32_e32 v163, 48, v163
	v_lshl_add_u32 v162, v162, 9, v163
	s_load_dwordx8 s[4:11], s[0:1], 0x0
	s_load_dwordx2 s[16:17], s[0:1], 0x20
	s_load_dwordx4 s[12:15], s[0:1], 0x30
	s_ashr_i32 s0, s2, 3
	s_mul_hi_i32 s18, s0, 0x55555556
	s_lshr_b32 s19, s18, 31
	s_add_i32 s21, s18, s19
	s_mul_i32 s18, s21, 0x3fffffd
	s_bfe_u32 s1, s2, 0x20001
	s_add_i32 s18, s18, s0
	s_lshl_b32 s2, s2, 5
	s_lshl_b32 s0, s18, 6
	s_and_b32 s2, s2, 32
	s_or_b32 s0, s0, s2
	s_lshl_b32 s2, s21, 1
	s_and_b32 s19, s2, -16
	s_lshl_b32 s2, s21, 4
	s_and_b32 s20, s2, 0x70
	s_mul_i32 s2, s1, 0xc0
	s_add_i32 s18, s0, s2
	s_mov_b32 s3, 0
	v_mov_b32_e32 v50, 0
	v_lshrrev_b32_e32 v142, 6, v0
	v_bfe_u32 v45, v0, 2, 4
	v_lshlrev_b32_e32 v1, 4, v0
	v_and_b32_e32 v34, 48, v1
	v_lshl_add_u32 v1, v142, 7, v45
	v_lshl_add_u32 v1, v1, 9, v34
	s_lshl_b32 s22, s18, 7
	s_add_i32 s22, s22, s19
	s_lshl_b32 s22, s22, 9
	s_lshl_b32 s2, s20, 2
	s_add_i32 s22, s22, s2
	s_waitcnt lgkmcnt(0)
	s_add_u32 s24, s4, s22
	s_addc_u32 s25, s5, 0
	s_add_u32 s26, s24, 0x40000
	s_addc_u32 s27, s25, 0
	s_add_u32 s28, s26, 0x40000
	s_addc_u32 s29, s27, 0
	s_add_u32 s30, s28, 0x40000
	s_addc_u32 s31, s29, 0
	s_add_u32 s32, s30, 0x40000
	s_addc_u32 s33, s31, 0
	s_add_u32 s34, s32, 0x40000
	s_addc_u32 s35, s33, 0
	s_add_u32 s36, s34, 0x40000
	s_addc_u32 s37, s35, 0
	s_add_u32 s38, s36, 0x40000
	s_addc_u32 s39, s37, 0
	v_readfirstlane_b32 s23, v142
	s_nop 3
	s_mul_i32 s23, s23, 0x410
	s_add_i32 m0, s23, 29120
	s_nop 0
	global_load_lds_dwordx4 v1, s[38:39]
	s_add_i32 m0, s23, 24960
	s_nop 0
	global_load_lds_dwordx4 v1, s[36:37]
	s_add_i32 m0, s23, 20800
	s_nop 0
	global_load_lds_dwordx4 v1, s[34:35]
	s_add_i32 m0, s23, 16640
	s_nop 0
	global_load_lds_dwordx4 v1, s[32:33]
	s_add_i32 m0, s23, 12480
	s_nop 0
	global_load_lds_dwordx4 v1, s[30:31]
	s_add_i32 m0, s23, 8320
	s_nop 0
	global_load_lds_dwordx4 v1, s[28:29]
	v_and_b32_e32 v35, 31, v0
	s_add_i32 m0, s23, 4160
	s_nop 0
	global_load_lds_dwordx4 v1, s[26:27]
	s_mov_b32 m0, s23
	s_nop 0
	global_load_lds_dwordx4 v1, s[24:25]
	v_lshlrev_b32_e32 v36, 1, v142
	v_bfe_u32 v37, v0, 2, 1
	v_add_u32_e32 v37, v36, v37
	v_lshrrev_b32_e32 v38, 1, v0
	v_and_b32_e32 v39, 3, v0
	v_and_or_b32 v38, v38, 12, v39
	v_lshl_add_u32 v37, v37, 7, v38
	v_bfe_u32 v39, v0, 5, 1
	v_lshlrev_b32_e32 v40, 4, v39
	v_lshl_add_u32 v37, v37, 5, v40
	v_add_u32_e32 v36, v36, v39
	v_lshlrev_b32_e32 v41, 1, v35
	v_lshl_add_u32 v38, v36, 9, v41
	v_or_b32_e32 v41, v41, v39
	v_lshlrev_b32_e32 v41, 4, v41
	v_lshlrev_b32_e32 v42, 2, v35
	s_lshl_b32 s70, s1, 2
	s_add_i32 s71, s70, 1
	s_add_i32 s72, s70, 3
	s_lshl_b32 s73, s20, 7
	s_add_i32 s73, s73, s19
	s_lshl_b32 s74, s71, 14
	s_add_i32 s74, s74, s73
	s_lshl_b32 s74, s74, 5
	s_lshl_b32 s75, s72, 14
	s_add_i32 s75, s75, s73
	s_lshl_b32 s75, s75, 5
	s_add_u32 s76, s6, s74
	s_addc_u32 s77, s7, 0
	s_add_u32 s78, s6, s75
	s_addc_u32 s79, s7, 0
	s_add_u32 s80, s76, 0x8000
	s_addc_u32 s81, s77, 0
	s_add_u32 s82, s78, 0x8000
	s_addc_u32 s83, s79, 0
	s_lshr_b32 s84, s0, 5
	s_mul_i32 s85, s71, 6
	s_add_i32 s85, s85, s84
	s_lshl_b32 s85, s85, 10
	s_mul_i32 s86, s72, 6
	s_add_i32 s86, s86, s84
	s_lshl_b32 s86, s86, 10
	s_lshl_b32 s87, s20, 3
	s_lshr_b32 s88, s19, 4
	s_add_i32 s87, s87, s88
	s_add_i32 s85, s85, s87
	s_lshl_b32 s85, s85, 6
	s_add_i32 s86, s86, s87
	s_lshl_b32 s86, s86, 6
	s_add_u32 s88, s12, s85
	s_addc_u32 s89, s13, 0
	s_add_u32 s90, s12, s86
	s_addc_u32 s91, s13, 0
	s_add_u32 s92, s88, 0x1000
	s_addc_u32 s93, s89, 0
	s_add_u32 s94, s90, 0x1000
	s_addc_u32 s95, s91, 0
	s_lshl_b32 s70, s0, 2
	s_add_u32 s84, s16, s70
	s_addc_u32 s85, s17, 0
	global_load_dword v94, v42, s[84:85]
	global_load_dwordx4 v[58:61], v37, s[80:81]
	global_load_dwordx4 v[62:65], v37, s[82:83]
	global_load_ushort v145, v38, s[92:93]
	global_load_ushort v146, v38, s[94:95]
	s_add_i32 s70, s0, 0xc0
	s_lshl_b32 s70, s70, 5
	s_add_u32 s84, s8, s70
	s_addc_u32 s85, s9, 0
	global_load_dwordx4 v[66:69], v41, s[84:85]
	s_add_i32 s70, s0, 0x240
	s_lshl_b32 s70, s70, 5
	s_add_u32 s86, s8, s70
	s_addc_u32 s87, s9, 0
	global_load_dwordx4 v[70:73], v41, s[86:87]
	s_add_i32 s70, s0, 0x240
	s_lshl_b32 s70, s70, 2
	s_add_u32 s84, s10, s70
	s_addc_u32 s85, s11, 0
	global_load_dword v92, v42, s[84:85]
	s_add_i32 s70, s0, 0xc0
	s_lshl_b32 s70, s70, 2
	s_add_u32 s86, s10, s70
	s_addc_u32 s87, s11, 0
	global_load_dword v96, v42, s[86:87]
	global_load_ushort v150, v38, s[90:91]
	global_load_ushort v151, v38, s[88:89]
	global_load_dwordx4 v[74:77], v37, s[78:79]
	global_load_dwordx4 v[78:81], v37, s[76:77]
	v_or_b32_e32 v36, s0, v35
	v_ashrrev_i32_e32 v37, 31, v36
	v_lshlrev_b64 v[38:39], 2, v[36:37]
	v_lshlrev_b32_e32 v89, 1, v142
	v_and_b32_e32 v1, 3, v0
	v_lshrrev_b32_e32 v37, 1, v0
	v_lshl_add_u64 v[40:41], s[16:17], 0, v[38:39]
	v_and_or_b32 v144, v37, 12, v1
	v_or_b32_e32 v1, s20, v89
	v_bfe_u32 v143, v0, 2, 1
	v_lshlrev_b32_e32 v40, 1, v35
	v_mov_b32_e32 v41, v50
	v_or_b32_e32 v37, 8, v1
	v_bfe_u32 v95, v0, 5, 1
	s_lshl_b32 s4, s1, 16
	v_lshl_add_u64 v[86:87], s[12:13], 0, v[40:41]
	v_or_b32_e32 v51, s19, v144
	v_or_b32_e32 v40, v37, v143
	v_lshlrev_b32_e32 v82, 4, v95
	v_mov_b32_e32 v83, v50
	s_ashr_i32 s5, s0, 5
	s_or_b32 s0, s4, 0x4000
	v_lshl_add_u32 v42, v40, 7, v51
	v_lshl_add_u64 v[84:85], s[6:7], 0, v[82:83]
	s_or_b32 s2, s4, 0xc000
	s_mul_i32 s7, s1, 24
	v_add_u32_e32 v40, s0, v42
	s_or_b32 s1, s7, 6
	v_ashrrev_i32_e32 v41, 31, v40
	v_add_u32_e32 v42, s2, v42
	s_add_i32 s6, s5, 12
	s_ashr_i32 s12, s21, 3
	s_add_i32 s13, s1, s5
	v_lshlrev_b64 v[40:41], 5, v[40:41]
	v_ashrrev_i32_e32 v43, 31, v42
	v_or_b32_e32 v37, v37, v95
	s_lshl_b32 s13, s13, 10
	s_add_i32 s1, s1, s6
	v_lshl_add_u64 v[40:41], v[84:85], 0, v[40:41]
	v_lshlrev_b64 v[42:43], 5, v[42:43]
	v_lshl_add_u32 v37, v37, 3, s12
	s_lshl_b32 s1, s1, 10
	v_lshl_add_u64 v[42:43], v[84:85], 0, v[42:43]
	v_add_u32_e32 v40, s13, v37
	v_ashrrev_i32_e32 v41, 31, v40
	v_add_u32_e32 v42, s1, v37
	v_lshlrev_b64 v[40:41], 6, v[40:41]
	v_ashrrev_i32_e32 v43, 31, v42
	v_lshl_or_b32 v88, v36, 1, v95
	v_lshl_add_u64 v[40:41], v[86:87], 0, v[40:41]
	v_lshlrev_b64 v[42:43], 6, v[42:43]
	v_add_u32_e32 v36, 0x180, v88
	v_lshl_add_u64 v[42:43], v[86:87], 0, v[42:43]
	v_ashrrev_i32_e32 v37, 31, v36
	v_add_u32_e32 v40, 0x480, v88
	v_lshl_add_u64 v[36:37], v[36:37], 4, s[8:9]
	v_ashrrev_i32_e32 v41, 31, v40
	v_lshl_add_u64 v[40:41], v[40:41], 4, s[8:9]
	v_or_b32_e32 v36, v1, v95
	v_lshl_add_u64 v[90:91], s[10:11], 0, v[38:39]
	v_lshl_add_u32 v38, v36, 3, s12
	v_add_u32_e32 v36, s1, v38
	v_ashrrev_i32_e32 v37, 31, v36
	v_add_u32_e32 v38, s13, v38
	v_lshlrev_b64 v[36:37], 6, v[36:37]
	v_ashrrev_i32_e32 v39, 31, v38
	v_or_b32_e32 v1, v1, v143
	v_lshl_add_u64 v[36:37], v[86:87], 0, v[36:37]
	v_lshlrev_b64 v[38:39], 6, v[38:39]
	v_lshl_add_u32 v1, v1, 7, v51
	v_lshl_add_u64 v[38:39], v[86:87], 0, v[38:39]
	v_add_u32_e32 v36, s2, v1
	v_ashrrev_i32_e32 v37, 31, v36
	v_add_u32_e32 v38, s0, v1
	v_lshlrev_b64 v[36:37], 5, v[36:37]
	v_ashrrev_i32_e32 v39, 31, v38
	v_lshl_add_u64 v[36:37], v[84:85], 0, v[36:37]
	v_lshlrev_b64 v[38:39], 5, v[38:39]
	v_lshl_add_u64 v[38:39], v[84:85], 0, v[38:39]
	v_and_b32_e32 v1, 63, v0
	v_cmp_gt_u32_e32 vcc, 32, v1
	v_bfrev_b32_e32 v1, 60
	v_mul_u32_u24_e32 v83, 0x210, v35
	v_mov_b32_e32 v36, 0x3c00
	v_cndmask_b32_e64 v56, v1, 0, vcc
	v_mul_u32_u24_e32 v1, 0x410, v35
	v_lshl_or_b32 v35, v95, 1, v83
	v_cndmask_b32_e64 v53, v36, 0, vcc
	v_add_u32_e32 v148, 0x8200, v35
	v_mul_u32_u24_e32 v35, 0x410, v142
	v_lshlrev_b32_e32 v36, 6, v45
	v_add3_u32 v34, v35, v36, v34
	s_waitcnt vmcnt(13)
	s_waitcnt lgkmcnt(0)
	s_barrier
	v_mov_b32_e32 v51, v50
	v_mov_b32_e32 v52, v50
	v_mov_b32_e32 v54, v50
	v_mov_b32_e32 v55, v50
	v_mov_b32_e32 v57, v50
	v_lshl_or_b32 v147, v95, 2, v1
	s_mov_b64 s[0:1], -1
	s_mov_b32 s10, 0x7f61b1e6
	s_mov_b32 s11, 0x42800000
	s_waitcnt vmcnt(5)
	v_mov_b32_e32 v93, v92
	s_waitcnt vmcnt(4)
	v_mov_b32_e32 v97, v96
	s_branch .LBB3_3
